# v69 plus cmp-attn importance head-sums fused into v_add_f32_dpp (bit-identical) and the sel-attn selection-mask load requested before the first unit barrier
# speedup vs baseline: 1.0062x; 1.0003x over previous
; __device__ __forceinline__ float dpp_xor1(float v) { return __int_as_float(__builtin_amdgcn_update_dpp(0, __float_as_int(v), 0xB1, 0xf, 0xf, false)); }
; __device__ __forceinline__ float dpp_xor2(float v) { return __int_as_float(__builtin_amdgcn_update_dpp(0, __float_as_int(v), 0x4E, 0xf, 0xf, false)); }
;     ...
;                         if (MODE == 2 && pass == 1) {
;                             float base[4], im3[4], rot[4];
; #pragma unroll
;                             for (int kt = 0; kt < 4; ++kt) { float im[4];
; #pragma unroll
;                                 for (int r = 0; r < 4; ++r) { float v = p[kt][r]; v += dpp_xor1(v); v += dpp_xor2(v); im[r] = v; }
;                                 base[kt] = 2.0f * (im[0] + im[1] + im[2]) + im[3]; im3[kt] = im[3]; }
; #pragma unroll
;                             for (int kt = 0; kt < 4; ++kt) rot[kt] = __shfl(im3[kt], (lane + 48) & 63);
; #pragma unroll
;                             for (int kt = 0; kt < 4; ++kt) { const float pv3 = q > 0 ? rot[kt] : (kt == 0 ? carry3[qd] : rot[kt > 0 ? kt - 1 : 0]);
;                                 const int jg = (p0 + 16 * kt + 4 * q) >> 2;
;                                 if (hr == 0 && jg < 256) sscore[(tq - t0) * SSTR + jg] = base[kt] + pv3; }
;                             carry3[qd] = rot[3];
.LBB0_892:
	v_add_u32_e32 v126, s27, v141
	v_ashrrev_i32_e32 v127, 2, v126
	s_and_b64 vcc, exec, s[36:37]
	v_cmp_gt_i32_e64 s[14:15], s23, v127
	s_cbranch_vccnz .LBB0_902
	v_add_f32_dpp v128, v217, v217 quad_perm:[1,0,3,2] row_mask:0xf bank_mask:0xf bound_ctrl:1
	v_mov_b32_e32 v122, 0
	v_mov_b32_e32 v123, 0
	v_add_f32_dpp v243, v128, v128 quad_perm:[2,3,0,1] row_mask:0xf bank_mask:0xf bound_ctrl:1
	v_add_f32_dpp v128, v221, v221 quad_perm:[1,0,3,2] row_mask:0xf bank_mask:0xf bound_ctrl:1
	v_mov_b32_dpp v122, v150 quad_perm:[1,0,3,2] row_mask:0xf bank_mask:0xf
	v_mov_b32_dpp v123, v151 quad_perm:[1,0,3,2] row_mask:0xf bank_mask:0xf
	v_add_f32_dpp v241, v128, v128 quad_perm:[2,3,0,1] row_mask:0xf bank_mask:0xf bound_ctrl:1
	v_add_f32_dpp v128, v225, v225 quad_perm:[1,0,3,2] row_mask:0xf bank_mask:0xf bound_ctrl:1
	v_add_f32_dpp v249, v216, v216 quad_perm:[1,0,3,2] row_mask:0xf bank_mask:0xf bound_ctrl:1
	v_mov_b32_e32 v250, 0
	v_add_f32_dpp v164, v128, v128 quad_perm:[2,3,0,1] row_mask:0xf bank_mask:0xf bound_ctrl:1
	v_add_f32_dpp v128, v229, v229 quad_perm:[1,0,3,2] row_mask:0xf bank_mask:0xf bound_ctrl:1
	v_pk_add_f32 v[122:123], v[150:151], v[122:123]
	v_mov_b32_e32 v124, 0
	v_add_f32_dpp v132, v128, v128 quad_perm:[2,3,0,1] row_mask:0xf bank_mask:0xf bound_ctrl:1
	v_and_or_b32 v128, v244, 64, v139
	v_lshlrev_b32_e32 v128, 2, v128
	ds_bpermute_b32 v192, v128, v243
	ds_bpermute_b32 v248, v128, v241
	ds_bpermute_b32 v134, v128, v164
	ds_bpermute_b32 v128, v128, v132
	v_mov_b32_e32 v125, 0
	v_add_f32_dpp v238, v218, v218 quad_perm:[1,0,3,2] row_mask:0xf bank_mask:0xf bound_ctrl:1
	v_add_f32_dpp v240, v219, v219 quad_perm:[1,0,3,2] row_mask:0xf bank_mask:0xf bound_ctrl:1
	v_add_f32_dpp v246, v220, v220 quad_perm:[1,0,3,2] row_mask:0xf bank_mask:0xf bound_ctrl:1
	v_add_f32_dpp v135, v222, v222 quad_perm:[1,0,3,2] row_mask:0xf bank_mask:0xf bound_ctrl:1
	v_add_f32_dpp v137, v223, v223 quad_perm:[1,0,3,2] row_mask:0xf bank_mask:0xf bound_ctrl:1
	v_add_f32_dpp v235, v224, v224 quad_perm:[1,0,3,2] row_mask:0xf bank_mask:0xf bound_ctrl:1
	v_add_f32_dpp v129, v226, v226 quad_perm:[1,0,3,2] row_mask:0xf bank_mask:0xf bound_ctrl:1
	v_add_f32_dpp v131, v227, v227 quad_perm:[1,0,3,2] row_mask:0xf bank_mask:0xf bound_ctrl:1
	v_add_f32_dpp v191, v228, v228 quad_perm:[1,0,3,2] row_mask:0xf bank_mask:0xf bound_ctrl:1
	v_mov_b32_dpp v250, v249 quad_perm:[2,3,0,1] row_mask:0xf bank_mask:0xf
	v_mov_b32_dpp v124, v122 quad_perm:[2,3,0,1] row_mask:0xf bank_mask:0xf
	v_mov_b32_dpp v125, v123 quad_perm:[2,3,0,1] row_mask:0xf bank_mask:0xf
	v_add_f32_dpp v239, v238, v238 quad_perm:[2,3,0,1] row_mask:0xf bank_mask:0xf bound_ctrl:1
	v_add_f32_dpp v245, v240, v240 quad_perm:[2,3,0,1] row_mask:0xf bank_mask:0xf bound_ctrl:1
	v_add_f32_dpp v247, v246, v246 quad_perm:[2,3,0,1] row_mask:0xf bank_mask:0xf bound_ctrl:1
	v_add_f32_dpp v136, v135, v135 quad_perm:[2,3,0,1] row_mask:0xf bank_mask:0xf bound_ctrl:1
	v_add_f32_dpp v165, v137, v137 quad_perm:[2,3,0,1] row_mask:0xf bank_mask:0xf bound_ctrl:1
	v_add_f32_dpp v237, v235, v235 quad_perm:[2,3,0,1] row_mask:0xf bank_mask:0xf bound_ctrl:1
	v_add_f32_dpp v130, v129, v129 quad_perm:[2,3,0,1] row_mask:0xf bank_mask:0xf bound_ctrl:1
	v_add_f32_dpp v133, v131, v131 quad_perm:[2,3,0,1] row_mask:0xf bank_mask:0xf bound_ctrl:1
	v_add_f32_dpp v236, v191, v191 quad_perm:[2,3,0,1] row_mask:0xf bank_mask:0xf bound_ctrl:1
	s_and_b64 s[14:15], s[2:3], s[14:15]
	s_and_saveexec_b64 s[4:5], s[14:15]
	s_cbranch_execz .LBB0_895
	v_pk_add_f32 v[122:123], v[122:123], v[124:125]
	v_add_f32_e32 v124, v249, v250
	v_add_f32_e32 v122, v122, v124
	v_add_f32_e32 v122, v122, v123
	v_fmac_f32_e32 v243, 2.0, v122
	s_waitcnt lgkmcnt(3)
	v_cndmask_b32_e64 v123, v192, v234, s[0:1]
	v_lshl_add_u32 v122, v127, 2, v231
	v_add_f32_e32 v123, v243, v123
	ds_write_b32 v122, v123 offset:16384
.LBB0_895:
	s_or_b64 exec, exec, s[4:5]
	v_add_u32_e32 v122, 16, v126
	v_ashrrev_i32_e32 v122, 2, v122
	v_cmp_gt_i32_e32 vcc, s23, v122
	s_and_b64 s[14:15], s[2:3], vcc
	s_and_saveexec_b64 s[4:5], s[14:15]
	s_cbranch_execz .LBB0_897
	v_add_f32_e32 v123, v239, v245
	v_add_f32_e32 v123, v123, v247
	v_fmac_f32_e32 v241, 2.0, v123
	s_waitcnt lgkmcnt(2)
	v_cndmask_b32_e64 v123, v248, v192, s[0:1]
	v_add_f32_e32 v123, v241, v123
	v_lshl_add_u32 v122, v122, 2, v231
	ds_write_b32 v122, v123 offset:16384
.LBB0_897:
	s_or_b64 exec, exec, s[4:5]
	v_add_u32_e32 v122, 32, v126
	v_ashrrev_i32_e32 v122, 2, v122
	v_cmp_gt_i32_e32 vcc, s23, v122
	s_and_b64 s[14:15], s[2:3], vcc
	s_and_saveexec_b64 s[4:5], s[14:15]
	s_cbranch_execz .LBB0_899
	v_add_f32_e32 v123, v136, v165
	v_add_f32_e32 v123, v123, v237
	v_fmac_f32_e32 v164, 2.0, v123
	s_waitcnt lgkmcnt(1)
	v_cndmask_b32_e64 v123, v134, v248, s[0:1]
	v_add_f32_e32 v123, v164, v123
	v_lshl_add_u32 v122, v122, 2, v231
	ds_write_b32 v122, v123 offset:16384
.LBB0_899:
	s_or_b64 exec, exec, s[4:5]
	v_add_u32_e32 v122, 48, v126
	v_ashrrev_i32_e32 v122, 2, v122
	v_cmp_gt_i32_e32 vcc, s23, v122
	s_and_b64 s[14:15], s[2:3], vcc
	s_and_saveexec_b64 s[4:5], s[14:15]
	s_cbranch_execz .LBB0_901
	v_add_f32_e32 v123, v130, v133
	v_add_f32_e32 v123, v123, v236
	v_fmac_f32_e32 v132, 2.0, v123
	s_waitcnt lgkmcnt(0)
	v_cndmask_b32_e64 v123, v128, v134, s[0:1]
	v_add_f32_e32 v123, v132, v123
	v_lshl_add_u32 v122, v122, 2, v231
	ds_write_b32 v122, v123 offset:16384

; __device__ __forceinline__ float dpp_xor1(float v) { return __int_as_float(__builtin_amdgcn_update_dpp(0, __float_as_int(v), 0xB1, 0xf, 0xf, false)); }
; __device__ __forceinline__ float dpp_xor2(float v) { return __int_as_float(__builtin_amdgcn_update_dpp(0, __float_as_int(v), 0x4E, 0xf, 0xf, false)); }
;     ...
;                         if (MODE == 2 && pass == 1) {
;                             float base[4], im3[4], rot[4];
; #pragma unroll
;                             for (int kt = 0; kt < 4; ++kt) { float im[4];
; #pragma unroll
;                                 for (int r = 0; r < 4; ++r) { float v = p[kt][r]; v += dpp_xor1(v); v += dpp_xor2(v); im[r] = v; }
;                                 base[kt] = 2.0f * (im[0] + im[1] + im[2]) + im[3]; im3[kt] = im[3]; }
; #pragma unroll
;                             for (int kt = 0; kt < 4; ++kt) rot[kt] = __shfl(im3[kt], (lane + 48) & 63);
; #pragma unroll
;                             for (int kt = 0; kt < 4; ++kt) { const float pv3 = q > 0 ? rot[kt] : (kt == 0 ? carry3[qd] : rot[kt > 0 ? kt - 1 : 0]);
;                                 const int jg = (p0 + 16 * kt + 4 * q) >> 2;
;                                 if (hr == 0 && jg < 256) sscore[(tq - t0) * SSTR + jg] = base[kt] + pv3; }
;                             carry3[qd] = rot[3];
.LBB0_908:
	s_and_b64 vcc, exec, s[36:37]
	s_cbranch_vccnz .LBB0_918
	v_add_f32_dpp v94, v217, v217 quad_perm:[1,0,3,2] row_mask:0xf bank_mask:0xf bound_ctrl:1
	v_mov_b32_e32 v90, 0
	v_mov_b32_e32 v91, 0
	v_add_f32_dpp v120, v94, v94 quad_perm:[2,3,0,1] row_mask:0xf bank_mask:0xf bound_ctrl:1
	v_add_f32_dpp v94, v221, v221 quad_perm:[1,0,3,2] row_mask:0xf bank_mask:0xf bound_ctrl:1
	v_mov_b32_dpp v90, v150 quad_perm:[1,0,3,2] row_mask:0xf bank_mask:0xf
	v_mov_b32_dpp v91, v151 quad_perm:[1,0,3,2] row_mask:0xf bank_mask:0xf
	v_add_f32_dpp v113, v94, v94 quad_perm:[2,3,0,1] row_mask:0xf bank_mask:0xf bound_ctrl:1
	v_add_f32_dpp v94, v225, v225 quad_perm:[1,0,3,2] row_mask:0xf bank_mask:0xf bound_ctrl:1
	v_add_f32_dpp v118, v216, v216 quad_perm:[1,0,3,2] row_mask:0xf bank_mask:0xf bound_ctrl:1
	v_mov_b32_e32 v119, 0
	v_add_f32_dpp v105, v94, v94 quad_perm:[2,3,0,1] row_mask:0xf bank_mask:0xf bound_ctrl:1
	v_add_f32_dpp v94, v229, v229 quad_perm:[1,0,3,2] row_mask:0xf bank_mask:0xf bound_ctrl:1
	v_pk_add_f32 v[90:91], v[150:151], v[90:91]
	v_mov_b32_e32 v92, 0
	v_add_f32_dpp v98, v94, v94 quad_perm:[2,3,0,1] row_mask:0xf bank_mask:0xf bound_ctrl:1
	v_and_or_b32 v94, v244, 64, v139
	v_lshlrev_b32_e32 v94, 2, v94
	ds_bpermute_b32 v121, v94, v120
	ds_bpermute_b32 v117, v94, v113
	ds_bpermute_b32 v101, v94, v105
	ds_bpermute_b32 v94, v94, v98
	v_mov_b32_e32 v93, 0
	v_add_f32_dpp v110, v218, v218 quad_perm:[1,0,3,2] row_mask:0xf bank_mask:0xf bound_ctrl:1
	v_add_f32_dpp v112, v219, v219 quad_perm:[1,0,3,2] row_mask:0xf bank_mask:0xf bound_ctrl:1
	v_add_f32_dpp v115, v220, v220 quad_perm:[1,0,3,2] row_mask:0xf bank_mask:0xf bound_ctrl:1
	v_add_f32_dpp v102, v222, v222 quad_perm:[1,0,3,2] row_mask:0xf bank_mask:0xf bound_ctrl:1
	v_add_f32_dpp v104, v223, v223 quad_perm:[1,0,3,2] row_mask:0xf bank_mask:0xf bound_ctrl:1
	v_add_f32_dpp v108, v224, v224 quad_perm:[1,0,3,2] row_mask:0xf bank_mask:0xf bound_ctrl:1
	v_add_f32_dpp v95, v226, v226 quad_perm:[1,0,3,2] row_mask:0xf bank_mask:0xf bound_ctrl:1
	v_add_f32_dpp v97, v227, v227 quad_perm:[1,0,3,2] row_mask:0xf bank_mask:0xf bound_ctrl:1
	v_add_f32_dpp v100, v228, v228 quad_perm:[1,0,3,2] row_mask:0xf bank_mask:0xf bound_ctrl:1
	v_cmp_gt_i32_e32 vcc, s23, v127
	v_mov_b32_dpp v119, v118 quad_perm:[2,3,0,1] row_mask:0xf bank_mask:0xf
	v_mov_b32_dpp v92, v90 quad_perm:[2,3,0,1] row_mask:0xf bank_mask:0xf
	v_mov_b32_dpp v93, v91 quad_perm:[2,3,0,1] row_mask:0xf bank_mask:0xf
	v_add_f32_dpp v111, v110, v110 quad_perm:[2,3,0,1] row_mask:0xf bank_mask:0xf bound_ctrl:1
	v_add_f32_dpp v114, v112, v112 quad_perm:[2,3,0,1] row_mask:0xf bank_mask:0xf bound_ctrl:1
	v_add_f32_dpp v116, v115, v115 quad_perm:[2,3,0,1] row_mask:0xf bank_mask:0xf bound_ctrl:1
	v_add_f32_dpp v103, v102, v102 quad_perm:[2,3,0,1] row_mask:0xf bank_mask:0xf bound_ctrl:1
	v_add_f32_dpp v106, v104, v104 quad_perm:[2,3,0,1] row_mask:0xf bank_mask:0xf bound_ctrl:1
	v_add_f32_dpp v109, v108, v108 quad_perm:[2,3,0,1] row_mask:0xf bank_mask:0xf bound_ctrl:1
	v_add_f32_dpp v96, v95, v95 quad_perm:[2,3,0,1] row_mask:0xf bank_mask:0xf bound_ctrl:1
	v_add_f32_dpp v99, v97, v97 quad_perm:[2,3,0,1] row_mask:0xf bank_mask:0xf bound_ctrl:1
	v_add_f32_dpp v107, v100, v100 quad_perm:[2,3,0,1] row_mask:0xf bank_mask:0xf bound_ctrl:1
	s_and_b64 s[14:15], s[2:3], vcc
	s_and_saveexec_b64 s[4:5], s[14:15]
	s_cbranch_execz .LBB0_911
	v_pk_add_f32 v[90:91], v[90:91], v[92:93]
	v_add_f32_e32 v92, v118, v119
	v_add_f32_e32 v90, v90, v92
	v_add_f32_e32 v90, v90, v91
	v_fmac_f32_e32 v120, 2.0, v90
	s_waitcnt lgkmcnt(3)
	v_cndmask_b32_e64 v91, v121, v233, s[0:1]
	v_lshl_add_u32 v90, v127, 2, v232
	v_add_f32_e32 v91, v120, v91
	ds_write_b32 v90, v91 offset:16384
.LBB0_911:
	s_or_b64 exec, exec, s[4:5]
	v_add_u32_e32 v90, 16, v126
	v_ashrrev_i32_e32 v90, 2, v90
	v_cmp_gt_i32_e32 vcc, s23, v90
	s_and_b64 s[14:15], s[2:3], vcc
	s_and_saveexec_b64 s[4:5], s[14:15]
	s_cbranch_execz .LBB0_913
	v_add_f32_e32 v91, v111, v114
	v_add_f32_e32 v91, v91, v116
	v_fmac_f32_e32 v113, 2.0, v91
	s_waitcnt lgkmcnt(2)
	v_cndmask_b32_e64 v91, v117, v121, s[0:1]
	v_add_f32_e32 v91, v113, v91
	v_lshl_add_u32 v90, v90, 2, v232
	ds_write_b32 v90, v91 offset:16384
.LBB0_913:
	s_or_b64 exec, exec, s[4:5]
	v_add_u32_e32 v90, 32, v126
	v_ashrrev_i32_e32 v90, 2, v90
	v_cmp_gt_i32_e32 vcc, s23, v90
	s_and_b64 s[14:15], s[2:3], vcc
	s_and_saveexec_b64 s[4:5], s[14:15]
	s_cbranch_execz .LBB0_915
	v_add_f32_e32 v91, v103, v106
	v_add_f32_e32 v91, v91, v109
	v_fmac_f32_e32 v105, 2.0, v91
	s_waitcnt lgkmcnt(1)
	v_cndmask_b32_e64 v91, v101, v117, s[0:1]
	v_add_f32_e32 v91, v105, v91
	v_lshl_add_u32 v90, v90, 2, v232
	ds_write_b32 v90, v91 offset:16384
.LBB0_915:
	s_or_b64 exec, exec, s[4:5]
	v_add_u32_e32 v90, 48, v126
	v_ashrrev_i32_e32 v90, 2, v90
	v_cmp_gt_i32_e32 vcc, s23, v90
	s_and_b64 s[14:15], s[2:3], vcc
	s_and_saveexec_b64 s[4:5], s[14:15]
	s_cbranch_execz .LBB0_917
	v_add_f32_e32 v91, v96, v99
	v_add_f32_e32 v91, v91, v107
	v_fmac_f32_e32 v98, 2.0, v91
	s_waitcnt lgkmcnt(0)
	v_cndmask_b32_e64 v91, v94, v101, s[0:1]
	v_add_f32_e32 v91, v98, v91
	v_lshl_add_u32 v90, v90, 2, v232
	ds_write_b32 v90, v91 offset:16384
